# v12 plus 64-byte alignment of the 14 GEMM K-loop headers
# speedup vs baseline: 1.0714x; 1.0714x over previous
;     DI bool next(int i, Unit& u) const { u.aux = 0; return tile_map(i, nM, nN, G, c, u.pm, u.pn); }
;     DI size_t a_off(const Unit& u) const { return (size_t)u.pm * astep; }
;     DI size_t b_off(const Unit& u) const { return (size_t)u.pn * bstep; }
;     DI bool next(int i, Unit& u) const { int pn; u.aux = 0; if (!tile_map(i, NTOK / 256, 16, G, c, u.pm, pn)) return false; u.pn = pn < 8 ? pn : pn + 8; return true; }
;     DI size_t a_off(const Unit& u) const { return (size_t)u.pm * (256 * D_ * 2); }
;     DI size_t b_off(const Unit& u) const { return (size_t)u.pn * (256 * D_ * 2); }
;     DI bool next(int i, Unit& u) const { int pn2; if (!tile_map(i, NTOK / 256, 8, G, c, u.pm, pn2)) return false; u.pn = pn2 >> 1; u.aux = pn2 & 1; return true; }
;     DI size_t a_off(const Unit& u) const { return (size_t)u.pm * (256 * D_ * 2) + (size_t)u.aux * (D_ / 2 * 2); }
;     DI size_t b_off(const Unit& u) const { return (size_t)(12 + u.pn) * (256 * D_ * 2) + (size_t)u.aux * (D_ / 2 * 2); }
;     DI bool next(int i, Unit& u) const { u.aux = 0; return tile_map(i, 8, NTOK / 256, G, c, u.pm, u.pn); }
;     DI size_t a_off(const Unit& u) const { const int phys = u.pm < 4 ? 8 + u.pm : 20 + u.pm; return (size_t)phys * (256 * D_ * 2); }
;     DI size_t b_off(const Unit& u) const { return (size_t)u.pn * (256 * D_ * 2); }
;     DI int nt(const Unit& u) const { return (u.aux & 8) ? PLED / 64 : ((u.aux & 4) ? (D_ / 2) / 64 : D_ / 64); }
;     DI bool next(int i, Unit& u) const { u.aux = i & 1; return tile_map(i >> 1, NTOK / 256, D_ / 256, G, c, u.pm, u.pn); }
;     DI size_t a_off(const Unit& u) const { return (size_t)u.pm * astep; }
; template <class Epi, class Sched, bool ALIGN_EPI, bool FP8 = false>
; DI void gemm_phase(LAS unsigned char* lds, const Gemm g, const Sched& S, const Epi& E) {
;     ...
;     for (;;) {
;         const bool has_next = S.next(ui + 1, nxt);
;         const char* nA = has_next ? (const char*)g.A + S.a_off(nxt) : cA; const char* nB = has_next ? (const char*)g.Bt + S.b_off(nxt) : cB;
;         for (int t = 0; t < nt; t += 2) {
;             if constexpr (Epi::MID) { if (t == (nt >> 1)) E.mid(acc, cur, wr, wc, fr, fq); }
;             const bool last = (t == nt - 2);
;             const char* a1 = cA + (size_t)(t + 1) * kstep;
;             const char* a2 = last ? nA : cA + (size_t)(t + 2) * kstep; const char* b2 = last ? nB : cB + (size_t)(t + 2) * kstep;
.LBB0_254:
	s_add_i32 s20, s81, -2
	s_mov_b32 s51, 0
	s_mov_b64 s[56:57], 0
	.p2alignl 6, 3212836864

;     DI bool next(int i, Unit& u) const { u.aux = 0; return tile_map(i, nM, nN, G, c, u.pm, u.pn); }
;     DI size_t a_off(const Unit& u) const { return (size_t)u.pm * astep; }
;     DI size_t b_off(const Unit& u) const { return (size_t)u.pn * bstep; }
;     DI bool next(int i, Unit& u) const { int pn; u.aux = 0; if (!tile_map(i, NTOK / 256, 16, G, c, u.pm, pn)) return false; u.pn = pn < 8 ? pn : pn + 8; return true; }
;     DI size_t a_off(const Unit& u) const { return (size_t)u.pm * (256 * D_ * 2); }
;     DI size_t b_off(const Unit& u) const { return (size_t)u.pn * (256 * D_ * 2); }
;     DI bool next(int i, Unit& u) const { int pn2; if (!tile_map(i, NTOK / 256, 8, G, c, u.pm, pn2)) return false; u.pn = pn2 >> 1; u.aux = pn2 & 1; return true; }
;     DI size_t a_off(const Unit& u) const { return (size_t)u.pm * (256 * D_ * 2) + (size_t)u.aux * (D_ / 2 * 2); }
;     DI size_t b_off(const Unit& u) const { return (size_t)(12 + u.pn) * (256 * D_ * 2) + (size_t)u.aux * (D_ / 2 * 2); }
;     DI bool next(int i, Unit& u) const { u.aux = 0; return tile_map(i, 8, NTOK / 256, G, c, u.pm, u.pn); }
;     DI size_t a_off(const Unit& u) const { const int phys = u.pm < 4 ? 8 + u.pm : 20 + u.pm; return (size_t)phys * (256 * D_ * 2); }
;     DI size_t b_off(const Unit& u) const { return (size_t)u.pn * (256 * D_ * 2); }
;     DI int nt(const Unit& u) const { return (u.aux & 8) ? PLED / 64 : ((u.aux & 4) ? (D_ / 2) / 64 : D_ / 64); }
;     DI bool next(int i, Unit& u) const { u.aux = i & 1; return tile_map(i >> 1, NTOK / 256, D_ / 256, G, c, u.pm, u.pn); }
; template <class Epi, class Sched, bool ALIGN_EPI, bool FP8 = false>
; DI void gemm_phase(LAS unsigned char* lds, const Gemm g, const Sched& S, const Epi& E) {
;     ...
;         const bool has_next = S.next(ui + 1, nxt);
;         const char* nA = has_next ? (const char*)g.A + S.a_off(nxt) : cA; const char* nB = has_next ? (const char*)g.Bt + S.b_off(nxt) : cB;
;     ...
; #pragma unroll
;         for (int a = 0; a < 2; ++a)
; #pragma unroll
;             for (int b = 0; b < 2; ++b)
; #pragma unroll
;                 for (int m = 0; m < 4; ++m)
; #pragma unroll
;                     for (int n = 0; n < 2; ++n) acc[a][b][m][n] = (f32x4){0.f, 0.f, 0.f, 0.f};
;         cur = nxt; cA = nA; cB = nB; ++ui;
;         if constexpr (sched_vark<Sched>::value) nt = S.nt(cur);
.LBB0_297:
	s_ashr_i32 s43, s42, 31
	s_lshl_b64 s[44:45], s[42:43], 19
	s_add_u32 s44, s36, s44
	s_addc_u32 s45, s37, s45
	s_and_b64 s[46:47], s[4:5], exec
	s_cselect_b32 s43, s45, s51
	s_cselect_b32 s87, s44, s50
	s_ashr_i32 s41, s40, 31
	s_lshl_b64 s[46:47], s[40:41], 19
	s_add_u32 s46, s39, s46
	s_addc_u32 s47, s60, s47
	s_and_b64 s[54:55], s[4:5], exec
	s_cselect_b32 s41, s47, s53
	s_cselect_b32 s88, s46, s52
	s_add_u32 s89, s52, 0x100
	v_mov_b32_e32 v0, 0
	s_addc_u32 s90, s53, 0
	s_mov_b32 s91, -2
	v_mov_b32_e32 v1, v0
	v_mov_b32_e32 v2, v0
	v_mov_b32_e32 v3, v0
	v_mov_b32_e32 v4, v0
	v_mov_b32_e32 v5, v0
	v_mov_b32_e32 v6, v0
	v_mov_b32_e32 v7, v0
	s_waitcnt vmcnt(19)
	v_mov_b32_e32 v16, v0
	v_mov_b32_e32 v17, v0
	v_mov_b32_e32 v18, v0
	v_mov_b32_e32 v19, v0
	s_waitcnt vmcnt(18)
	v_mov_b32_e32 v20, v0
	v_mov_b32_e32 v21, v0
	v_mov_b32_e32 v22, v0
	v_mov_b32_e32 v23, v0
	s_waitcnt vmcnt(15)
	v_mov_b32_e32 v32, v0
	v_mov_b32_e32 v33, v0
	v_mov_b32_e32 v34, v0
	v_mov_b32_e32 v35, v0
	s_waitcnt vmcnt(14)
	v_mov_b32_e32 v36, v0
	v_mov_b32_e32 v37, v0
	v_mov_b32_e32 v38, v0
	v_mov_b32_e32 v39, v0
	v_mov_b32_e32 v48, v0
	v_mov_b32_e32 v49, v0
	v_mov_b32_e32 v50, v0
	v_mov_b32_e32 v51, v0
	v_mov_b32_e32 v52, v0
	v_mov_b32_e32 v53, v0
	v_mov_b32_e32 v54, v0
	v_mov_b32_e32 v55, v0
	v_mov_b32_e32 v8, v0
	v_mov_b32_e32 v9, v0
	v_mov_b32_e32 v10, v0
	v_mov_b32_e32 v11, v0
	v_mov_b32_e32 v12, v0
	v_mov_b32_e32 v13, v0
	v_mov_b32_e32 v14, v0
	v_mov_b32_e32 v15, v0
	v_mov_b32_e32 v24, v0
	v_mov_b32_e32 v25, v0
	v_mov_b32_e32 v26, v0
	v_mov_b32_e32 v27, v0
	v_mov_b32_e32 v28, v0
	v_mov_b32_e32 v29, v0
	v_mov_b32_e32 v30, v0
	v_mov_b32_e32 v31, v0
	v_mov_b32_e32 v40, v0
	v_mov_b32_e32 v41, v0
	v_mov_b32_e32 v42, v0
	v_mov_b32_e32 v43, v0
	v_mov_b32_e32 v44, v0
	v_mov_b32_e32 v45, v0
	v_mov_b32_e32 v46, v0
	v_mov_b32_e32 v47, v0
	s_waitcnt vmcnt(13)
	v_mov_b32_e32 v56, v0
	v_mov_b32_e32 v57, v0
	v_mov_b32_e32 v58, v0
	v_mov_b32_e32 v59, v0
	s_waitcnt vmcnt(12)
	v_mov_b32_e32 v60, v0
	v_mov_b32_e32 v61, v0
	v_mov_b32_e32 v62, v0
	v_mov_b32_e32 v63, v0
	v_mov_b32_e32 v64, v0
	v_mov_b32_e32 v65, v0
	v_mov_b32_e32 v66, v0
	v_mov_b32_e32 v67, v0
	v_mov_b32_e32 v68, v0
	v_mov_b32_e32 v69, v0
	v_mov_b32_e32 v70, v0
	v_mov_b32_e32 v71, v0
	s_waitcnt vmcnt(11)
	v_mov_b32_e32 v80, v0
	v_mov_b32_e32 v81, v0
	v_mov_b32_e32 v82, v0
	v_mov_b32_e32 v83, v0
	v_mov_b32_e32 v84, v0
	v_mov_b32_e32 v85, v0
	v_mov_b32_e32 v86, v0
	v_mov_b32_e32 v87, v0
	s_waitcnt vmcnt(9)
	v_mov_b32_e32 v96, v0
	v_mov_b32_e32 v97, v0
	v_mov_b32_e32 v98, v0
	v_mov_b32_e32 v99, v0
	v_mov_b32_e32 v100, v0
	v_mov_b32_e32 v101, v0
	v_mov_b32_e32 v102, v0
	v_mov_b32_e32 v103, v0
	v_mov_b32_e32 v128, v0
	v_mov_b32_e32 v129, v0
	v_mov_b32_e32 v130, v0
	v_mov_b32_e32 v131, v0
	v_mov_b32_e32 v132, v0
	v_mov_b32_e32 v133, v0
	v_mov_b32_e32 v134, v0
	v_mov_b32_e32 v135, v0
	v_mov_b32_e32 v72, v0
	v_mov_b32_e32 v73, v0
	v_mov_b32_e32 v74, v0
	v_mov_b32_e32 v75, v0
	v_mov_b32_e32 v76, v0
	v_mov_b32_e32 v77, v0
	v_mov_b32_e32 v78, v0
	v_mov_b32_e32 v79, v0
	v_mov_b32_e32 v88, v0
	v_mov_b32_e32 v89, v0
	v_mov_b32_e32 v90, v0
	v_mov_b32_e32 v91, v0
	v_mov_b32_e32 v92, v0
	v_mov_b32_e32 v93, v0
	v_mov_b32_e32 v94, v0
	v_mov_b32_e32 v95, v0
	v_mov_b32_e32 v120, v0
	v_mov_b32_e32 v121, v0
	v_mov_b32_e32 v122, v0
	v_mov_b32_e32 v123, v0
	v_mov_b32_e32 v124, v0
	v_mov_b32_e32 v125, v0
	v_mov_b32_e32 v126, v0
	v_mov_b32_e32 v127, v0
	v_mov_b32_e32 v136, v0
	v_mov_b32_e32 v137, v0
	v_mov_b32_e32 v138, v0
	v_mov_b32_e32 v139, v0
	v_mov_b32_e32 v140, v0
	v_mov_b32_e32 v141, v0
	v_mov_b32_e32 v142, v0
	v_mov_b32_e32 v143, v0
	.p2alignl 6, 3212836864

;     DI bool next(int i, Unit& u) const { u.aux = 0; return tile_map(i, nM, nN, G, c, u.pm, u.pn); }
;     DI size_t a_off(const Unit& u) const { return (size_t)u.pm * astep; }
;     DI size_t b_off(const Unit& u) const { return (size_t)u.pn * bstep; }
;     DI bool next(int i, Unit& u) const { int pn; u.aux = 0; if (!tile_map(i, NTOK / 256, 16, G, c, u.pm, pn)) return false; u.pn = pn < 8 ? pn : pn + 8; return true; }
;     DI size_t a_off(const Unit& u) const { return (size_t)u.pm * (256 * D_ * 2); }
;     DI size_t b_off(const Unit& u) const { return (size_t)u.pn * (256 * D_ * 2); }
;     DI bool next(int i, Unit& u) const { int pn2; if (!tile_map(i, NTOK / 256, 8, G, c, u.pm, pn2)) return false; u.pn = pn2 >> 1; u.aux = pn2 & 1; return true; }
;     DI size_t a_off(const Unit& u) const { return (size_t)u.pm * (256 * D_ * 2) + (size_t)u.aux * (D_ / 2 * 2); }
;     DI size_t b_off(const Unit& u) const { return (size_t)(12 + u.pn) * (256 * D_ * 2) + (size_t)u.aux * (D_ / 2 * 2); }
;     DI bool next(int i, Unit& u) const { u.aux = 0; return tile_map(i, 8, NTOK / 256, G, c, u.pm, u.pn); }
;     DI size_t a_off(const Unit& u) const { const int phys = u.pm < 4 ? 8 + u.pm : 20 + u.pm; return (size_t)phys * (256 * D_ * 2); }
;     DI size_t b_off(const Unit& u) const { return (size_t)u.pn * (256 * D_ * 2); }
;     DI int nt(const Unit& u) const { return (u.aux & 8) ? PLED / 64 : ((u.aux & 4) ? (D_ / 2) / 64 : D_ / 64); }
; template <class Epi, class Sched, bool ALIGN_EPI, bool FP8 = false>
; DI void gemm_phase(LAS unsigned char* lds, const Gemm g, const Sched& S, const Epi& E) {
;     ...
;         const bool has_next = S.next(ui + 1, nxt);
;         const char* nA = has_next ? (const char*)g.A + S.a_off(nxt) : cA; const char* nB = has_next ? (const char*)g.Bt + S.b_off(nxt) : cB;
;         for (int t = 0; t < nt; t += 2) {
;             if constexpr (Epi::MID) { if (t == (nt >> 1)) E.mid(acc, cur, wr, wc, fr, fq); }
;     ...
; #pragma unroll
;         for (int a = 0; a < 2; ++a)
; #pragma unroll
;             for (int b = 0; b < 2; ++b)
; #pragma unroll
;                 for (int m = 0; m < 4; ++m)
; #pragma unroll
;                     for (int n = 0; n < 2; ++n) acc[a][b][m][n] = (f32x4){0.f, 0.f, 0.f, 0.f};
;         cur = nxt; cA = nA; cB = nB; ++ui;
;         if constexpr (sched_vark<Sched>::value) nt = S.nt(cur);
.LBB0_487:
	s_ashr_i32 s21, s20, 31
	s_lshl_b64 s[22:23], s[20:21], 20
	s_add_u32 s22, s35, s22
	s_addc_u32 s23, s36, s23
	s_and_b64 s[24:25], s[4:5], exec
	s_cselect_b32 s21, s23, s27
	s_cselect_b32 s65, s22, s26
	s_ashr_i32 s19, s18, 31
	s_lshl_b64 s[24:25], s[18:19], 20
	s_add_u32 s24, s37, s24
	s_addc_u32 s25, s39, s25
	s_and_b64 s[42:43], s[4:5], exec
	v_lshl_or_b32 v150, s29, 8, v159
	v_mov_b32_e32 v2, v0
	v_mov_b32_e32 v3, v0
	s_cselect_b32 s19, s25, s41
	s_cselect_b32 s66, s24, s40
	v_ashrrev_i32_e32 v151, 31, v150
	s_add_u32 s67, s40, 0x100
	v_mov_b32_e32 v1, v0
	v_mov_b64_e32 v[6:7], v[2:3]
	v_mov_b64_e32 v[10:11], v[2:3]
	s_waitcnt vmcnt(18)
	v_mov_b64_e32 v[22:23], v[2:3]
	s_waitcnt vmcnt(17)
	v_mov_b64_e32 v[26:27], v[2:3]
	s_waitcnt vmcnt(14)
	v_mov_b64_e32 v[38:39], v[2:3]
	v_mov_b64_e32 v[42:43], v[2:3]
	v_mov_b64_e32 v[54:55], v[2:3]
	s_waitcnt vmcnt(13)
	v_mov_b64_e32 v[58:59], v[2:3]
	v_mov_b64_e32 v[14:15], v[2:3]
	v_mov_b64_e32 v[18:19], v[2:3]
	v_mov_b64_e32 v[30:31], v[2:3]
	v_mov_b64_e32 v[34:35], v[2:3]
	v_mov_b64_e32 v[46:47], v[2:3]
	v_mov_b64_e32 v[50:51], v[2:3]
	s_waitcnt vmcnt(12)
	v_mov_b64_e32 v[62:63], v[2:3]
	v_mov_b64_e32 v[66:67], v[2:3]
	v_mov_b64_e32 v[70:71], v[2:3]
	v_mov_b64_e32 v[74:75], v[2:3]
	s_waitcnt vmcnt(11)
	v_mov_b64_e32 v[86:87], v[2:3]
	s_waitcnt vmcnt(10)
	v_mov_b64_e32 v[90:91], v[2:3]
	v_mov_b64_e32 v[102:103], v[2:3]
	s_waitcnt vmcnt(9)
	v_mov_b64_e32 v[106:107], v[2:3]
	v_mov_b64_e32 v[118:119], v[2:3]
	v_mov_b64_e32 v[122:123], v[2:3]
	v_mov_b64_e32 v[78:79], v[2:3]
	v_mov_b64_e32 v[82:83], v[2:3]
	v_mov_b64_e32 v[94:95], v[2:3]
	v_mov_b64_e32 v[98:99], v[2:3]
	s_waitcnt vmcnt(8)
	v_mov_b64_e32 v[110:111], v[2:3]
	v_mov_b64_e32 v[114:115], v[2:3]
	v_mov_b64_e32 v[126:127], v[2:3]
	v_mov_b64_e32 v[130:131], v[2:3]
	v_lshl_add_u32 v148, s28, 8, v158
	v_lshl_add_u64 v[152:153], v[150:151], 1, s[10:11]
	s_addc_u32 s68, s41, 0
	s_mov_b32 s69, -2
	v_mov_b64_e32 v[4:5], v[0:1]
	v_mov_b64_e32 v[8:9], v[0:1]
	v_mov_b64_e32 v[20:21], v[0:1]
	v_mov_b64_e32 v[24:25], v[0:1]
	v_mov_b64_e32 v[36:37], v[0:1]
	v_mov_b64_e32 v[40:41], v[0:1]
	v_mov_b64_e32 v[52:53], v[0:1]
	v_mov_b64_e32 v[56:57], v[0:1]
	v_mov_b64_e32 v[12:13], v[0:1]
	v_mov_b64_e32 v[16:17], v[0:1]
	v_mov_b64_e32 v[28:29], v[0:1]
	v_mov_b64_e32 v[32:33], v[0:1]
	v_mov_b64_e32 v[44:45], v[0:1]
	v_mov_b64_e32 v[48:49], v[0:1]
	v_mov_b64_e32 v[60:61], v[0:1]
	v_mov_b64_e32 v[64:65], v[0:1]
	v_mov_b64_e32 v[68:69], v[0:1]
	v_mov_b64_e32 v[72:73], v[0:1]
	v_mov_b64_e32 v[84:85], v[0:1]
	v_mov_b64_e32 v[88:89], v[0:1]
	v_mov_b64_e32 v[100:101], v[0:1]
	v_mov_b64_e32 v[104:105], v[0:1]
	v_mov_b64_e32 v[116:117], v[0:1]
	v_mov_b64_e32 v[120:121], v[0:1]
	v_mov_b64_e32 v[76:77], v[0:1]
	v_mov_b64_e32 v[80:81], v[0:1]
	v_mov_b64_e32 v[92:93], v[0:1]
	v_mov_b64_e32 v[96:97], v[0:1]
	v_mov_b64_e32 v[108:109], v[0:1]
	v_mov_b64_e32 v[112:113], v[0:1]
	v_mov_b64_e32 v[124:125], v[0:1]
	v_mov_b64_e32 v[128:129], v[0:1]
	s_cmp_lg_u32 s69, 14
	s_cbranch_scc1 .LBB0_489
	.p2alignl 6, 3212836864

;     DI bool next(int i, Unit& u) const { u.aux = 0; return tile_map(i, nM, nN, G, c, u.pm, u.pn); }
;     DI size_t a_off(const Unit& u) const { return (size_t)u.pm * astep; }
;     DI size_t b_off(const Unit& u) const { return (size_t)u.pn * bstep; }
;     DI bool next(int i, Unit& u) const { int pn; u.aux = 0; if (!tile_map(i, NTOK / 256, 16, G, c, u.pm, pn)) return false; u.pn = pn < 8 ? pn : pn + 8; return true; }
;     DI size_t a_off(const Unit& u) const { return (size_t)u.pm * (256 * D_ * 2); }
;     DI size_t b_off(const Unit& u) const { return (size_t)u.pn * (256 * D_ * 2); }
;     DI bool next(int i, Unit& u) const { int pn2; if (!tile_map(i, NTOK / 256, 8, G, c, u.pm, pn2)) return false; u.pn = pn2 >> 1; u.aux = pn2 & 1; return true; }
;     DI size_t a_off(const Unit& u) const { return (size_t)u.pm * (256 * D_ * 2) + (size_t)u.aux * (D_ / 2 * 2); }
;     DI size_t b_off(const Unit& u) const { return (size_t)(12 + u.pn) * (256 * D_ * 2) + (size_t)u.aux * (D_ / 2 * 2); }
;     DI bool next(int i, Unit& u) const { u.aux = 0; return tile_map(i, 8, NTOK / 256, G, c, u.pm, u.pn); }
;     DI size_t a_off(const Unit& u) const { const int phys = u.pm < 4 ? 8 + u.pm : 20 + u.pm; return (size_t)phys * (256 * D_ * 2); }
;     DI size_t b_off(const Unit& u) const { return (size_t)u.pn * (256 * D_ * 2); }
;     DI int nt(const Unit& u) const { return (u.aux & 8) ? PLED / 64 : ((u.aux & 4) ? (D_ / 2) / 64 : D_ / 64); }
;     DI bool next(int i, Unit& u) const { u.aux = i & 1; return tile_map(i >> 1, NTOK / 256, D_ / 256, G, c, u.pm, u.pn); }
; template <class Epi, class Sched, bool ALIGN_EPI, bool FP8 = false>
; DI void gemm_phase(LAS unsigned char* lds, const Gemm g, const Sched& S, const Epi& E) {
;     ...
;         const bool has_next = S.next(ui + 1, nxt);
;         const char* nA = has_next ? (const char*)g.A + S.a_off(nxt) : cA; const char* nB = has_next ? (const char*)g.Bt + S.b_off(nxt) : cB;
;     ...
; #pragma unroll
;         for (int a = 0; a < 2; ++a)
; #pragma unroll
;             for (int b = 0; b < 2; ++b)
; #pragma unroll
;                 for (int m = 0; m < 4; ++m)
; #pragma unroll
;                     for (int n = 0; n < 2; ++n) acc[a][b][m][n] = (f32x4){0.f, 0.f, 0.f, 0.f};
;         cur = nxt; cA = nA; cB = nB; ++ui;
;         if constexpr (sched_vark<Sched>::value) nt = S.nt(cur);
.LBB0_568:
	s_ashr_i32 s57, s56, 31
	s_lshl_b64 s[58:59], s[56:57], 20
	s_add_u32 s58, s17, s58
	s_addc_u32 s59, s35, s59
	s_and_b64 s[60:61], s[4:5], exec
	s_cselect_b32 s57, s59, s65
	s_cselect_b32 s93, s58, s64
	s_ashr_i32 s55, s54, 31
	s_lshl_b64 s[60:61], s[54:55], 20
	s_add_u32 s60, s36, s60
	s_addc_u32 s61, s37, s61
	s_and_b64 s[68:69], s[4:5], exec
	s_cselect_b32 s55, s61, s67
	s_cselect_b32 s94, s60, s66
	s_add_u32 s95, s66, 0x100
	v_mov_b32_e32 v0, 0
	s_addc_u32 s96, s67, 0
	s_mov_b32 s97, -2
	v_mov_b32_e32 v1, v0
	v_mov_b32_e32 v2, v0
	v_mov_b32_e32 v3, v0
	v_mov_b32_e32 v4, v0
	v_mov_b32_e32 v5, v0
	v_mov_b32_e32 v6, v0
	v_mov_b32_e32 v7, v0
	v_mov_b32_e32 v16, v0
	v_mov_b32_e32 v17, v0
	v_mov_b32_e32 v18, v0
	v_mov_b32_e32 v19, v0
	v_mov_b32_e32 v20, v0
	v_mov_b32_e32 v21, v0
	v_mov_b32_e32 v22, v0
	v_mov_b32_e32 v23, v0
	s_waitcnt vmcnt(15)
	v_mov_b32_e32 v32, v0
	v_mov_b32_e32 v33, v0
	v_mov_b32_e32 v34, v0
	v_mov_b32_e32 v35, v0
	s_waitcnt vmcnt(14)
	v_mov_b32_e32 v36, v0
	v_mov_b32_e32 v37, v0
	v_mov_b32_e32 v38, v0
	v_mov_b32_e32 v39, v0
	v_mov_b32_e32 v48, v0
	v_mov_b32_e32 v49, v0
	v_mov_b32_e32 v50, v0
	v_mov_b32_e32 v51, v0
	v_mov_b32_e32 v52, v0
	v_mov_b32_e32 v53, v0
	v_mov_b32_e32 v54, v0
	v_mov_b32_e32 v55, v0
	v_mov_b32_e32 v8, v0
	v_mov_b32_e32 v9, v0
	v_mov_b32_e32 v10, v0
	v_mov_b32_e32 v11, v0
	v_mov_b32_e32 v12, v0
	v_mov_b32_e32 v13, v0
	v_mov_b32_e32 v14, v0
	v_mov_b32_e32 v15, v0
	v_mov_b32_e32 v24, v0
	v_mov_b32_e32 v25, v0
	v_mov_b32_e32 v26, v0
	v_mov_b32_e32 v27, v0
	v_mov_b32_e32 v28, v0
	v_mov_b32_e32 v29, v0
	v_mov_b32_e32 v30, v0
	v_mov_b32_e32 v31, v0
	v_mov_b32_e32 v40, v0
	v_mov_b32_e32 v41, v0
	v_mov_b32_e32 v42, v0
	v_mov_b32_e32 v43, v0
	v_mov_b32_e32 v44, v0
	v_mov_b32_e32 v45, v0
	v_mov_b32_e32 v46, v0
	v_mov_b32_e32 v47, v0
	s_waitcnt vmcnt(13)
	v_mov_b32_e32 v56, v0
	v_mov_b32_e32 v57, v0
	v_mov_b32_e32 v58, v0
	v_mov_b32_e32 v59, v0
	s_waitcnt vmcnt(12)
	v_mov_b32_e32 v60, v0
	v_mov_b32_e32 v61, v0
	v_mov_b32_e32 v62, v0
	v_mov_b32_e32 v63, v0
	v_mov_b32_e32 v64, v0
	v_mov_b32_e32 v65, v0
	v_mov_b32_e32 v66, v0
	v_mov_b32_e32 v67, v0
	v_mov_b32_e32 v68, v0
	v_mov_b32_e32 v69, v0
	v_mov_b32_e32 v70, v0
	v_mov_b32_e32 v71, v0
	s_waitcnt vmcnt(11)
	v_mov_b32_e32 v80, v0
	v_mov_b32_e32 v81, v0
	v_mov_b32_e32 v82, v0
	v_mov_b32_e32 v83, v0
	v_mov_b32_e32 v84, v0
	v_mov_b32_e32 v85, v0
	v_mov_b32_e32 v86, v0
	v_mov_b32_e32 v87, v0
	s_waitcnt vmcnt(9)
	v_mov_b32_e32 v96, v0
	v_mov_b32_e32 v97, v0
	v_mov_b32_e32 v98, v0
	v_mov_b32_e32 v99, v0
	v_mov_b32_e32 v100, v0
	v_mov_b32_e32 v101, v0
	v_mov_b32_e32 v102, v0
	v_mov_b32_e32 v103, v0
	s_waitcnt vmcnt(8)
	v_mov_b32_e32 v112, v0
	v_mov_b32_e32 v113, v0
	v_mov_b32_e32 v114, v0
	v_mov_b32_e32 v115, v0
	v_mov_b32_e32 v116, v0
	v_mov_b32_e32 v117, v0
	v_mov_b32_e32 v118, v0
	v_mov_b32_e32 v119, v0
	v_mov_b32_e32 v72, v0
	v_mov_b32_e32 v73, v0
	v_mov_b32_e32 v74, v0
	v_mov_b32_e32 v75, v0
	v_mov_b32_e32 v76, v0
	v_mov_b32_e32 v77, v0
	v_mov_b32_e32 v78, v0
	v_mov_b32_e32 v79, v0
	v_mov_b32_e32 v88, v0
	v_mov_b32_e32 v89, v0
	v_mov_b32_e32 v90, v0
	v_mov_b32_e32 v91, v0
	v_mov_b32_e32 v92, v0
	v_mov_b32_e32 v93, v0
	v_mov_b32_e32 v94, v0
	v_mov_b32_e32 v95, v0
	v_mov_b32_e32 v104, v0
	v_mov_b32_e32 v105, v0
	v_mov_b32_e32 v106, v0
	v_mov_b32_e32 v107, v0
	v_mov_b32_e32 v108, v0
	v_mov_b32_e32 v109, v0
	v_mov_b32_e32 v110, v0
	v_mov_b32_e32 v111, v0
	v_mov_b32_e32 v120, v0
	v_mov_b32_e32 v121, v0
	v_mov_b32_e32 v122, v0
	v_mov_b32_e32 v123, v0
	v_mov_b32_e32 v124, v0
	v_mov_b32_e32 v125, v0
	v_mov_b32_e32 v126, v0
	v_mov_b32_e32 v127, v0
	.p2alignl 6, 3212836864

;     DI bool next(int i, Unit& u) const { u.aux = 0; return tile_map(i, nM, nN, G, c, u.pm, u.pn); }
;     DI size_t a_off(const Unit& u) const { return (size_t)u.pm * astep; }
;     DI size_t b_off(const Unit& u) const { return (size_t)u.pn * bstep; }
;     DI bool next(int i, Unit& u) const { int pn; u.aux = 0; if (!tile_map(i, NTOK / 256, 16, G, c, u.pm, pn)) return false; u.pn = pn < 8 ? pn : pn + 8; return true; }
;     DI size_t a_off(const Unit& u) const { return (size_t)u.pm * (256 * D_ * 2); }
;     DI size_t b_off(const Unit& u) const { return (size_t)u.pn * (256 * D_ * 2); }
;     DI bool next(int i, Unit& u) const { int pn2; if (!tile_map(i, NTOK / 256, 8, G, c, u.pm, pn2)) return false; u.pn = pn2 >> 1; u.aux = pn2 & 1; return true; }
;     DI size_t a_off(const Unit& u) const { return (size_t)u.pm * (256 * D_ * 2) + (size_t)u.aux * (D_ / 2 * 2); }
;     DI size_t b_off(const Unit& u) const { return (size_t)(12 + u.pn) * (256 * D_ * 2) + (size_t)u.aux * (D_ / 2 * 2); }
;     DI bool next(int i, Unit& u) const { u.aux = 0; return tile_map(i, 8, NTOK / 256, G, c, u.pm, u.pn); }
;     DI size_t a_off(const Unit& u) const { const int phys = u.pm < 4 ? 8 + u.pm : 20 + u.pm; return (size_t)phys * (256 * D_ * 2); }
;     DI size_t b_off(const Unit& u) const { return (size_t)u.pn * (256 * D_ * 2); }
;     DI int nt(const Unit& u) const { return (u.aux & 8) ? PLED / 64 : ((u.aux & 4) ? (D_ / 2) / 64 : D_ / 64); }
;     DI bool next(int i, Unit& u) const { u.aux = i & 1; return tile_map(i >> 1, NTOK / 256, D_ / 256, G, c, u.pm, u.pn); }
; template <class Epi, class Sched, bool ALIGN_EPI, bool FP8 = false>
; DI void gemm_phase(LAS unsigned char* lds, const Gemm g, const Sched& S, const Epi& E) {
;     ...
;         const bool has_next = S.next(ui + 1, nxt);
;         const char* nA = has_next ? (const char*)g.A + S.a_off(nxt) : cA; const char* nB = has_next ? (const char*)g.Bt + S.b_off(nxt) : cB;
;     ...
; #pragma unroll
;         for (int a = 0; a < 2; ++a)
; #pragma unroll
;             for (int b = 0; b < 2; ++b)
; #pragma unroll
;                 for (int m = 0; m < 4; ++m)
; #pragma unroll
;                     for (int n = 0; n < 2; ++n) acc[a][b][m][n] = (f32x4){0.f, 0.f, 0.f, 0.f};
;         cur = nxt; cA = nA; cB = nB; ++ui;
;         if constexpr (sched_vark<Sched>::value) nt = S.nt(cur);
.LBB0_699:
	s_ashr_i32 s17, s16, 31
	s_lshl_b64 s[18:19], s[16:17], 20
	s_add_u32 s18, s3, s18
	s_addc_u32 s19, s35, s19
	s_and_b64 s[20:21], s[4:5], exec
	s_cselect_b32 s17, s19, s25
	s_cselect_b32 s67, s18, s24
	s_ashr_i32 s13, s12, 31
	s_lshl_b64 s[20:21], s[12:13], 20
	s_add_u32 s20, s36, s20
	s_addc_u32 s21, s37, s21
	s_and_b64 s[28:29], s[4:5], exec
	s_cselect_b32 s13, s21, s27
	s_cselect_b32 s68, s20, s26
	s_add_u32 s69, s26, 0x100
	v_mov_b32_e32 v0, 0
	s_addc_u32 s70, s27, 0
	s_mov_b32 s71, -2
	v_mov_b32_e32 v1, v0
	v_mov_b32_e32 v2, v0
	v_mov_b32_e32 v3, v0
	v_mov_b32_e32 v8, v0
	v_mov_b32_e32 v9, v0
	v_mov_b32_e32 v10, v0
	v_mov_b32_e32 v11, v0
	v_mov_b32_e32 v16, v0
	v_mov_b32_e32 v17, v0
	v_mov_b32_e32 v18, v0
	v_mov_b32_e32 v19, v0
	v_mov_b32_e32 v24, v0
	v_mov_b32_e32 v25, v0
	v_mov_b32_e32 v26, v0
	v_mov_b32_e32 v27, v0
	v_mov_b32_e32 v32, v0
	v_mov_b32_e32 v33, v0
	v_mov_b32_e32 v34, v0
	v_mov_b32_e32 v35, v0
	v_mov_b32_e32 v40, v0
	v_mov_b32_e32 v41, v0
	v_mov_b32_e32 v42, v0
	v_mov_b32_e32 v43, v0
	v_mov_b32_e32 v48, v0
	v_mov_b32_e32 v49, v0
	v_mov_b32_e32 v50, v0
	v_mov_b32_e32 v51, v0
	v_mov_b32_e32 v56, v0
	v_mov_b32_e32 v57, v0
	v_mov_b32_e32 v58, v0
	v_mov_b32_e32 v59, v0
	v_mov_b32_e32 v4, v0
	v_mov_b32_e32 v5, v0
	v_mov_b32_e32 v6, v0
	v_mov_b32_e32 v7, v0
	v_mov_b32_e32 v12, v0
	v_mov_b32_e32 v13, v0
	v_mov_b32_e32 v14, v0
	v_mov_b32_e32 v15, v0
	v_mov_b32_e32 v20, v0
	v_mov_b32_e32 v21, v0
	v_mov_b32_e32 v22, v0
	v_mov_b32_e32 v23, v0
	v_mov_b32_e32 v28, v0
	v_mov_b32_e32 v29, v0
	v_mov_b32_e32 v30, v0
	v_mov_b32_e32 v31, v0
	v_mov_b32_e32 v36, v0
	v_mov_b32_e32 v37, v0
	v_mov_b32_e32 v38, v0
	v_mov_b32_e32 v39, v0
	v_mov_b32_e32 v44, v0
	v_mov_b32_e32 v45, v0
	v_mov_b32_e32 v46, v0
	v_mov_b32_e32 v47, v0
	v_mov_b32_e32 v52, v0
	v_mov_b32_e32 v53, v0
	v_mov_b32_e32 v54, v0
	v_mov_b32_e32 v55, v0
	v_mov_b32_e32 v60, v0
	v_mov_b32_e32 v61, v0
	v_mov_b32_e32 v62, v0
	v_mov_b32_e32 v63, v0
	v_mov_b32_e32 v64, v0
	v_mov_b32_e32 v65, v0
	v_mov_b32_e32 v66, v0
	v_mov_b32_e32 v67, v0
	v_mov_b32_e32 v72, v0
	v_mov_b32_e32 v73, v0
	v_mov_b32_e32 v74, v0
	v_mov_b32_e32 v75, v0
	v_mov_b32_e32 v80, v0
	v_mov_b32_e32 v81, v0
	v_mov_b32_e32 v82, v0
	v_mov_b32_e32 v83, v0
	v_mov_b32_e32 v88, v0
	v_mov_b32_e32 v89, v0
	v_mov_b32_e32 v90, v0
	v_mov_b32_e32 v91, v0
	v_mov_b32_e32 v96, v0
	v_mov_b32_e32 v97, v0
	v_mov_b32_e32 v98, v0
	v_mov_b32_e32 v99, v0
	v_mov_b32_e32 v104, v0
	v_mov_b32_e32 v105, v0
	v_mov_b32_e32 v106, v0
	v_mov_b32_e32 v107, v0
	v_mov_b32_e32 v112, v0
	v_mov_b32_e32 v113, v0
	v_mov_b32_e32 v114, v0
	v_mov_b32_e32 v115, v0
	v_mov_b32_e32 v120, v0
	v_mov_b32_e32 v121, v0
	v_mov_b32_e32 v122, v0
	v_mov_b32_e32 v123, v0
	v_mov_b32_e32 v68, v0
	v_mov_b32_e32 v69, v0
	v_mov_b32_e32 v70, v0
	v_mov_b32_e32 v71, v0
	v_mov_b32_e32 v76, v0
	v_mov_b32_e32 v77, v0
	v_mov_b32_e32 v78, v0
	v_mov_b32_e32 v79, v0
	v_mov_b32_e32 v84, v0
	v_mov_b32_e32 v85, v0
	v_mov_b32_e32 v86, v0
	v_mov_b32_e32 v87, v0
	v_mov_b32_e32 v92, v0
	v_mov_b32_e32 v93, v0
	v_mov_b32_e32 v94, v0
	v_mov_b32_e32 v95, v0
	v_mov_b32_e32 v100, v0
	v_mov_b32_e32 v101, v0
	v_mov_b32_e32 v102, v0
	v_mov_b32_e32 v103, v0
	v_mov_b32_e32 v108, v0
	v_mov_b32_e32 v109, v0
	v_mov_b32_e32 v110, v0
	v_mov_b32_e32 v111, v0
	v_mov_b32_e32 v116, v0
	v_mov_b32_e32 v117, v0
	v_mov_b32_e32 v118, v0
	v_mov_b32_e32 v119, v0
	v_mov_b32_e32 v124, v0
	v_mov_b32_e32 v125, v0
	v_mov_b32_e32 v126, v0
	v_mov_b32_e32 v127, v0
	.p2alignl 6, 3212836864

;     DI bool next(int i, Unit& u) const { u.aux = 0; return tile_map(i, nM, nN, G, c, u.pm, u.pn); }
;     DI size_t a_off(const Unit& u) const { return (size_t)u.pm * astep; }
;     DI size_t b_off(const Unit& u) const { return (size_t)u.pn * bstep; }
;     DI bool next(int i, Unit& u) const { int pn; u.aux = 0; if (!tile_map(i, NTOK / 256, 16, G, c, u.pm, pn)) return false; u.pn = pn < 8 ? pn : pn + 8; return true; }
;     DI size_t a_off(const Unit& u) const { return (size_t)u.pm * (256 * D_ * 2); }
;     DI size_t b_off(const Unit& u) const { return (size_t)u.pn * (256 * D_ * 2); }
;     DI bool next(int i, Unit& u) const { int pn2; if (!tile_map(i, NTOK / 256, 8, G, c, u.pm, pn2)) return false; u.pn = pn2 >> 1; u.aux = pn2 & 1; return true; }
;     DI size_t a_off(const Unit& u) const { return (size_t)u.pm * (256 * D_ * 2) + (size_t)u.aux * (D_ / 2 * 2); }
;     DI size_t b_off(const Unit& u) const { return (size_t)(12 + u.pn) * (256 * D_ * 2) + (size_t)u.aux * (D_ / 2 * 2); }
;     DI bool next(int i, Unit& u) const { u.aux = 0; return tile_map(i, 8, NTOK / 256, G, c, u.pm, u.pn); }
;     DI size_t a_off(const Unit& u) const { const int phys = u.pm < 4 ? 8 + u.pm : 20 + u.pm; return (size_t)phys * (256 * D_ * 2); }
;     DI size_t b_off(const Unit& u) const { return (size_t)u.pn * (256 * D_ * 2); }
;     DI int nt(const Unit& u) const { return (u.aux & 8) ? PLED / 64 : ((u.aux & 4) ? (D_ / 2) / 64 : D_ / 64); }
;     DI bool next(int i, Unit& u) const { u.aux = i & 1; return tile_map(i >> 1, NTOK / 256, D_ / 256, G, c, u.pm, u.pn); }
; template <class Epi, class Sched, bool ALIGN_EPI, bool FP8 = false>
; DI void gemm_phase(LAS unsigned char* lds, const Gemm g, const Sched& S, const Epi& E) {
;     ...
;         const bool has_next = S.next(ui + 1, nxt);
;         const char* nA = has_next ? (const char*)g.A + S.a_off(nxt) : cA; const char* nB = has_next ? (const char*)g.Bt + S.b_off(nxt) : cB;
;     ...
; #pragma unroll
;         for (int a = 0; a < 2; ++a)
; #pragma unroll
;             for (int b = 0; b < 2; ++b)
; #pragma unroll
;                 for (int m = 0; m < 4; ++m)
; #pragma unroll
;                     for (int n = 0; n < 2; ++n) acc[a][b][m][n] = (f32x4){0.f, 0.f, 0.f, 0.f};
;         cur = nxt; cA = nA; cB = nB; ++ui;
;         if constexpr (sched_vark<Sched>::value) nt = S.nt(cur);
.LBB0_723:
	s_ashr_i32 s57, s56, 31
	s_lshl_b64 s[58:59], s[56:57], 20
	s_add_u32 s58, s3, s58
	s_addc_u32 s59, s35, s59
	s_and_b64 s[60:61], s[4:5], exec
	s_cselect_b32 s57, s59, s65
	s_cselect_b32 s94, s58, s64
	s_ashr_i32 s55, s54, 31
	s_lshl_b64 s[60:61], s[54:55], 20
	s_add_u32 s60, s37, s60
	s_addc_u32 s61, s39, s61
	s_and_b64 s[68:69], s[4:5], exec
	s_cselect_b32 s55, s61, s67
	s_cselect_b32 s95, s60, s66
	s_add_u32 s96, s66, 0x100
	v_mov_b32_e32 v0, 0
	s_addc_u32 s97, s67, 0
	s_mov_b32 vcc_lo, -2
	v_mov_b32_e32 v1, v0
	v_mov_b32_e32 v2, v0
	v_mov_b32_e32 v3, v0
	v_mov_b32_e32 v4, v0
	v_mov_b32_e32 v5, v0
	v_mov_b32_e32 v6, v0
	v_mov_b32_e32 v7, v0
	v_mov_b32_e32 v16, v0
	v_mov_b32_e32 v17, v0
	v_mov_b32_e32 v18, v0
	v_mov_b32_e32 v19, v0
	v_mov_b32_e32 v20, v0
	v_mov_b32_e32 v21, v0
	v_mov_b32_e32 v22, v0
	v_mov_b32_e32 v23, v0
	s_waitcnt vmcnt(15)
	v_mov_b32_e32 v32, v0
	v_mov_b32_e32 v33, v0
	v_mov_b32_e32 v34, v0
	v_mov_b32_e32 v35, v0
	s_waitcnt vmcnt(14)
	v_mov_b32_e32 v36, v0
	v_mov_b32_e32 v37, v0
	v_mov_b32_e32 v38, v0
	v_mov_b32_e32 v39, v0
	v_mov_b32_e32 v48, v0
	v_mov_b32_e32 v49, v0
	v_mov_b32_e32 v50, v0
	v_mov_b32_e32 v51, v0
	v_mov_b32_e32 v52, v0
	v_mov_b32_e32 v53, v0
	v_mov_b32_e32 v54, v0
	v_mov_b32_e32 v55, v0
	v_mov_b32_e32 v8, v0
	v_mov_b32_e32 v9, v0
	v_mov_b32_e32 v10, v0
	v_mov_b32_e32 v11, v0
	v_mov_b32_e32 v12, v0
	v_mov_b32_e32 v13, v0
	v_mov_b32_e32 v14, v0
	v_mov_b32_e32 v15, v0
	v_mov_b32_e32 v24, v0
	v_mov_b32_e32 v25, v0
	v_mov_b32_e32 v26, v0
	v_mov_b32_e32 v27, v0
	v_mov_b32_e32 v28, v0
	v_mov_b32_e32 v29, v0
	v_mov_b32_e32 v30, v0
	v_mov_b32_e32 v31, v0
	v_mov_b32_e32 v40, v0
	v_mov_b32_e32 v41, v0
	v_mov_b32_e32 v42, v0
	v_mov_b32_e32 v43, v0
	v_mov_b32_e32 v44, v0
	v_mov_b32_e32 v45, v0
	v_mov_b32_e32 v46, v0
	v_mov_b32_e32 v47, v0
	s_waitcnt vmcnt(13)
	v_mov_b32_e32 v56, v0
	v_mov_b32_e32 v57, v0
	v_mov_b32_e32 v58, v0
	v_mov_b32_e32 v59, v0
	s_waitcnt vmcnt(12)
	v_mov_b32_e32 v60, v0
	v_mov_b32_e32 v61, v0
	v_mov_b32_e32 v62, v0
	v_mov_b32_e32 v63, v0
	v_mov_b32_e32 v64, v0
	v_mov_b32_e32 v65, v0
	v_mov_b32_e32 v66, v0
	v_mov_b32_e32 v67, v0
	v_mov_b32_e32 v68, v0
	v_mov_b32_e32 v69, v0
	v_mov_b32_e32 v70, v0
	v_mov_b32_e32 v71, v0
	s_waitcnt vmcnt(11)
	v_mov_b32_e32 v80, v0
	v_mov_b32_e32 v81, v0
	v_mov_b32_e32 v82, v0
	v_mov_b32_e32 v83, v0
	v_mov_b32_e32 v84, v0
	v_mov_b32_e32 v85, v0
	v_mov_b32_e32 v86, v0
	v_mov_b32_e32 v87, v0
	s_waitcnt vmcnt(9)
	v_mov_b32_e32 v96, v0
	v_mov_b32_e32 v97, v0
	v_mov_b32_e32 v98, v0
	v_mov_b32_e32 v99, v0
	v_mov_b32_e32 v100, v0
	v_mov_b32_e32 v101, v0
	v_mov_b32_e32 v102, v0
	v_mov_b32_e32 v103, v0
	s_waitcnt vmcnt(8)
	v_mov_b32_e32 v112, v0
	v_mov_b32_e32 v113, v0
	v_mov_b32_e32 v114, v0
	v_mov_b32_e32 v115, v0
	v_mov_b32_e32 v116, v0
	v_mov_b32_e32 v117, v0
	v_mov_b32_e32 v118, v0
	v_mov_b32_e32 v119, v0
	v_mov_b32_e32 v72, v0
	v_mov_b32_e32 v73, v0
	v_mov_b32_e32 v74, v0
	v_mov_b32_e32 v75, v0
	v_mov_b32_e32 v76, v0
	v_mov_b32_e32 v77, v0
	v_mov_b32_e32 v78, v0
	v_mov_b32_e32 v79, v0
	v_mov_b32_e32 v88, v0
	v_mov_b32_e32 v89, v0
	v_mov_b32_e32 v90, v0
	v_mov_b32_e32 v91, v0
	v_mov_b32_e32 v92, v0
	v_mov_b32_e32 v93, v0
	v_mov_b32_e32 v94, v0
	v_mov_b32_e32 v95, v0
	v_mov_b32_e32 v104, v0
	v_mov_b32_e32 v105, v0
	v_mov_b32_e32 v106, v0
	v_mov_b32_e32 v107, v0
	v_mov_b32_e32 v108, v0
	v_mov_b32_e32 v109, v0
	v_mov_b32_e32 v110, v0
	v_mov_b32_e32 v111, v0
	v_mov_b32_e32 v120, v0
	v_mov_b32_e32 v121, v0
	v_mov_b32_e32 v122, v0
	v_mov_b32_e32 v123, v0
	v_mov_b32_e32 v124, v0
	v_mov_b32_e32 v125, v0
	v_mov_b32_e32 v126, v0
	v_mov_b32_e32 v127, v0
	.p2alignl 6, 3212836864

;     DI int nt(const Unit& u) const { return (u.aux & 8) ? PLED / 64 : ((u.aux & 4) ? (D_ / 2) / 64 : D_ / 64); }
; template <class Epi, class Sched, bool ALIGN_EPI, bool FP8 = false>
; DI void gemm_phase(LAS unsigned char* lds, const Gemm g, const Sched& S, const Epi& E) {
;     ...
; #pragma unroll
;         for (int a = 0; a < 2; ++a)
; #pragma unroll
;             for (int b = 0; b < 2; ++b)
; #pragma unroll
;                 for (int m = 0; m < 4; ++m)
; #pragma unroll
;                     for (int n = 0; n < 2; ++n) acc[a][b][m][n] = (f32x4){0.f, 0.f, 0.f, 0.f};
;         cur = nxt; cA = nA; cB = nB; ++ui;
;         if constexpr (sched_vark<Sched>::value) nt = S.nt(cur);
.LBB0_808:
	s_add_u32 s81, s50, 0x100
	v_mov_b32_e32 v0, 0
	s_addc_u32 s82, s51, 0
	s_mov_b32 s83, -2
	v_mov_b32_e32 v1, v0
	v_mov_b32_e32 v2, v0
	v_mov_b32_e32 v3, v0
	v_mov_b32_e32 v4, v0
	v_mov_b32_e32 v5, v0
	v_mov_b32_e32 v6, v0
	v_mov_b32_e32 v7, v0
	s_waitcnt vmcnt(19)
	v_mov_b32_e32 v16, v0
	v_mov_b32_e32 v17, v0
	v_mov_b32_e32 v18, v0
	v_mov_b32_e32 v19, v0
	s_waitcnt vmcnt(18)
	v_mov_b32_e32 v20, v0
	v_mov_b32_e32 v21, v0
	v_mov_b32_e32 v22, v0
	v_mov_b32_e32 v23, v0
	s_waitcnt vmcnt(15)
	v_mov_b32_e32 v32, v0
	v_mov_b32_e32 v33, v0
	v_mov_b32_e32 v34, v0
	v_mov_b32_e32 v35, v0
	s_waitcnt vmcnt(14)
	v_mov_b32_e32 v36, v0
	v_mov_b32_e32 v37, v0
	v_mov_b32_e32 v38, v0
	v_mov_b32_e32 v39, v0
	v_mov_b32_e32 v48, v0
	v_mov_b32_e32 v49, v0
	v_mov_b32_e32 v50, v0
	v_mov_b32_e32 v51, v0
	v_mov_b32_e32 v52, v0
	v_mov_b32_e32 v53, v0
	v_mov_b32_e32 v54, v0
	v_mov_b32_e32 v55, v0
	v_mov_b32_e32 v8, v0
	v_mov_b32_e32 v9, v0
	v_mov_b32_e32 v10, v0
	v_mov_b32_e32 v11, v0
	v_mov_b32_e32 v12, v0
	v_mov_b32_e32 v13, v0
	v_mov_b32_e32 v14, v0
	v_mov_b32_e32 v15, v0
	v_mov_b32_e32 v24, v0
	v_mov_b32_e32 v25, v0
	v_mov_b32_e32 v26, v0
	v_mov_b32_e32 v27, v0
	v_mov_b32_e32 v28, v0
	v_mov_b32_e32 v29, v0
	v_mov_b32_e32 v30, v0
	v_mov_b32_e32 v31, v0
	v_mov_b32_e32 v40, v0
	v_mov_b32_e32 v41, v0
	v_mov_b32_e32 v42, v0
	v_mov_b32_e32 v43, v0
	v_mov_b32_e32 v44, v0
	v_mov_b32_e32 v45, v0
	v_mov_b32_e32 v46, v0
	v_mov_b32_e32 v47, v0
	s_waitcnt vmcnt(13)
	v_mov_b32_e32 v56, v0
	v_mov_b32_e32 v57, v0
	v_mov_b32_e32 v58, v0
	v_mov_b32_e32 v59, v0
	s_waitcnt vmcnt(12)
	v_mov_b32_e32 v60, v0
	v_mov_b32_e32 v61, v0
	v_mov_b32_e32 v62, v0
	v_mov_b32_e32 v63, v0
	v_mov_b32_e32 v64, v0
	v_mov_b32_e32 v65, v0
	v_mov_b32_e32 v66, v0
	v_mov_b32_e32 v67, v0
	v_mov_b32_e32 v68, v0
	v_mov_b32_e32 v69, v0
	v_mov_b32_e32 v70, v0
	v_mov_b32_e32 v71, v0
	s_waitcnt vmcnt(11)
	v_mov_b32_e32 v80, v0
	v_mov_b32_e32 v81, v0
	v_mov_b32_e32 v82, v0
	v_mov_b32_e32 v83, v0
	v_mov_b32_e32 v84, v0
	v_mov_b32_e32 v85, v0
	v_mov_b32_e32 v86, v0
	v_mov_b32_e32 v87, v0
	s_waitcnt vmcnt(9)
	v_mov_b32_e32 v96, v0
	v_mov_b32_e32 v97, v0
	v_mov_b32_e32 v98, v0
	v_mov_b32_e32 v99, v0
	v_mov_b32_e32 v100, v0
	v_mov_b32_e32 v101, v0
	v_mov_b32_e32 v102, v0
	v_mov_b32_e32 v103, v0
	s_waitcnt vmcnt(8)
	v_mov_b32_e32 v112, v0
	v_mov_b32_e32 v113, v0
	v_mov_b32_e32 v114, v0
	v_mov_b32_e32 v115, v0
	v_mov_b32_e32 v116, v0
	v_mov_b32_e32 v117, v0
	v_mov_b32_e32 v118, v0
	v_mov_b32_e32 v119, v0
	v_mov_b32_e32 v72, v0
	v_mov_b32_e32 v73, v0
	v_mov_b32_e32 v74, v0
	v_mov_b32_e32 v75, v0
	v_mov_b32_e32 v76, v0
	v_mov_b32_e32 v77, v0
	v_mov_b32_e32 v78, v0
	v_mov_b32_e32 v79, v0
	v_mov_b32_e32 v88, v0
	v_mov_b32_e32 v89, v0
	v_mov_b32_e32 v90, v0
	v_mov_b32_e32 v91, v0
	v_mov_b32_e32 v92, v0
	v_mov_b32_e32 v93, v0
	v_mov_b32_e32 v94, v0
	v_mov_b32_e32 v95, v0
	v_mov_b32_e32 v104, v0
	v_mov_b32_e32 v105, v0
	v_mov_b32_e32 v106, v0
	v_mov_b32_e32 v107, v0
	v_mov_b32_e32 v108, v0
	v_mov_b32_e32 v109, v0
	v_mov_b32_e32 v110, v0
	v_mov_b32_e32 v111, v0
	v_mov_b32_e32 v120, v0
	v_mov_b32_e32 v121, v0
	v_mov_b32_e32 v122, v0
	v_mov_b32_e32 v123, v0
	v_mov_b32_e32 v124, v0
	v_mov_b32_e32 v125, v0
	v_mov_b32_e32 v126, v0
	v_mov_b32_e32 v127, v0
	.p2alignl 6, 3212836864

;     DI bool next(int i, Unit& u) const { u.aux = 0; return tile_map(i, nM, nN, G, c, u.pm, u.pn); }
;     DI size_t a_off(const Unit& u) const { return (size_t)u.pm * astep; }
;     DI size_t b_off(const Unit& u) const { return (size_t)u.pn * bstep; }
;     DI bool next(int i, Unit& u) const { int pn; u.aux = 0; if (!tile_map(i, NTOK / 256, 16, G, c, u.pm, pn)) return false; u.pn = pn < 8 ? pn : pn + 8; return true; }
;     DI size_t a_off(const Unit& u) const { return (size_t)u.pm * (256 * D_ * 2); }
;     DI size_t b_off(const Unit& u) const { return (size_t)u.pn * (256 * D_ * 2); }
;     DI bool next(int i, Unit& u) const { int pn2; if (!tile_map(i, NTOK / 256, 8, G, c, u.pm, pn2)) return false; u.pn = pn2 >> 1; u.aux = pn2 & 1; return true; }
;     DI size_t a_off(const Unit& u) const { return (size_t)u.pm * (256 * D_ * 2) + (size_t)u.aux * (D_ / 2 * 2); }
;     DI size_t b_off(const Unit& u) const { return (size_t)(12 + u.pn) * (256 * D_ * 2) + (size_t)u.aux * (D_ / 2 * 2); }
;     DI bool next(int i, Unit& u) const { u.aux = 0; return tile_map(i, 8, NTOK / 256, G, c, u.pm, u.pn); }
;     DI size_t a_off(const Unit& u) const { const int phys = u.pm < 4 ? 8 + u.pm : 20 + u.pm; return (size_t)phys * (256 * D_ * 2); }
;     DI size_t b_off(const Unit& u) const { return (size_t)u.pn * (256 * D_ * 2); }
;     DI int nt(const Unit& u) const { return (u.aux & 8) ? PLED / 64 : ((u.aux & 4) ? (D_ / 2) / 64 : D_ / 64); }
;     DI bool next(int i, Unit& u) const { u.aux = i & 1; return tile_map(i >> 1, NTOK / 256, D_ / 256, G, c, u.pm, u.pn); }
; template <class Epi, class Sched, bool ALIGN_EPI, bool FP8 = false>
; DI void gemm_phase(LAS unsigned char* lds, const Gemm g, const Sched& S, const Epi& E) {
;     ...
;         const bool has_next = S.next(ui + 1, nxt);
;         const char* nA = has_next ? (const char*)g.A + S.a_off(nxt) : cA; const char* nB = has_next ? (const char*)g.Bt + S.b_off(nxt) : cB;
;     ...
; #pragma unroll
;         for (int a = 0; a < 2; ++a)
; #pragma unroll
;             for (int b = 0; b < 2; ++b)
; #pragma unroll
;                 for (int m = 0; m < 4; ++m)
; #pragma unroll
;                     for (int n = 0; n < 2; ++n) acc[a][b][m][n] = (f32x4){0.f, 0.f, 0.f, 0.f};
;         cur = nxt; cA = nA; cB = nB; ++ui;
;         if constexpr (sched_vark<Sched>::value) nt = S.nt(cur);
.LBB0_1607:
	s_ashr_i32 s17, s16, 31
	s_lshl_b64 s[20:21], s[16:17], 19
	s_add_u32 s20, s35, s20
	s_addc_u32 s21, s36, s21
	s_and_b64 s[6:7], s[6:7], exec
	s_cselect_b32 s15, s21, s27
	s_cselect_b32 s17, s20, s26
	s_add_u32 s68, s28, 0x100
	v_mov_b32_e32 v0, 0
	s_addc_u32 s69, s29, 0
	s_mov_b32 s70, -2
	v_mov_b32_e32 v1, v0
	v_mov_b32_e32 v2, v0
	v_mov_b32_e32 v3, v0
	v_mov_b32_e32 v4, v0
	v_mov_b32_e32 v5, v0
	v_mov_b32_e32 v6, v0
	v_mov_b32_e32 v7, v0
	v_mov_b32_e32 v16, v0
	v_mov_b32_e32 v17, v0
	v_mov_b32_e32 v18, v0
	v_mov_b32_e32 v19, v0
	v_mov_b32_e32 v20, v0
	v_mov_b32_e32 v21, v0
	v_mov_b32_e32 v22, v0
	v_mov_b32_e32 v23, v0
	v_mov_b32_e32 v32, v0
	v_mov_b32_e32 v33, v0
	v_mov_b32_e32 v34, v0
	v_mov_b32_e32 v35, v0
	v_mov_b32_e32 v36, v0
	v_mov_b32_e32 v37, v0
	v_mov_b32_e32 v38, v0
	v_mov_b32_e32 v39, v0
	v_mov_b32_e32 v48, v0
	v_mov_b32_e32 v49, v0
	v_mov_b32_e32 v50, v0
	v_mov_b32_e32 v51, v0
	v_mov_b32_e32 v52, v0
	v_mov_b32_e32 v53, v0
	v_mov_b32_e32 v54, v0
	v_mov_b32_e32 v55, v0
	v_mov_b32_e32 v8, v0
	v_mov_b32_e32 v9, v0
	v_mov_b32_e32 v10, v0
	v_mov_b32_e32 v11, v0
	v_mov_b32_e32 v12, v0
	v_mov_b32_e32 v13, v0
	v_mov_b32_e32 v14, v0
	v_mov_b32_e32 v15, v0
	v_mov_b32_e32 v24, v0
	v_mov_b32_e32 v25, v0
	v_mov_b32_e32 v26, v0
	v_mov_b32_e32 v27, v0
	v_mov_b32_e32 v28, v0
	v_mov_b32_e32 v29, v0
	v_mov_b32_e32 v30, v0
	v_mov_b32_e32 v31, v0
	v_mov_b32_e32 v40, v0
	v_mov_b32_e32 v41, v0
	v_mov_b32_e32 v42, v0
	v_mov_b32_e32 v43, v0
	v_mov_b32_e32 v44, v0
	v_mov_b32_e32 v45, v0
	v_mov_b32_e32 v46, v0
	v_mov_b32_e32 v47, v0
	v_mov_b32_e32 v56, v0
	v_mov_b32_e32 v57, v0
	v_mov_b32_e32 v58, v0
	v_mov_b32_e32 v59, v0
	v_mov_b32_e32 v60, v0
	v_mov_b32_e32 v61, v0
	v_mov_b32_e32 v62, v0
	v_mov_b32_e32 v63, v0
	v_mov_b32_e32 v64, v0
	v_mov_b32_e32 v65, v0
	v_mov_b32_e32 v66, v0
	v_mov_b32_e32 v67, v0
	v_mov_b32_e32 v68, v0
	v_mov_b32_e32 v69, v0
	v_mov_b32_e32 v70, v0
	v_mov_b32_e32 v71, v0
	v_mov_b32_e32 v80, v0
	v_mov_b32_e32 v81, v0
	v_mov_b32_e32 v82, v0
	v_mov_b32_e32 v83, v0
	v_mov_b32_e32 v84, v0
	v_mov_b32_e32 v85, v0
	v_mov_b32_e32 v86, v0
	v_mov_b32_e32 v87, v0
	v_mov_b32_e32 v96, v0
	v_mov_b32_e32 v97, v0
	v_mov_b32_e32 v98, v0
	v_mov_b32_e32 v99, v0
	v_mov_b32_e32 v100, v0
	v_mov_b32_e32 v101, v0
	v_mov_b32_e32 v102, v0
	v_mov_b32_e32 v103, v0
	v_mov_b32_e32 v112, v0
	v_mov_b32_e32 v113, v0
	v_mov_b32_e32 v114, v0
	v_mov_b32_e32 v115, v0
	v_mov_b32_e32 v116, v0
	v_mov_b32_e32 v117, v0
	v_mov_b32_e32 v118, v0
	v_mov_b32_e32 v119, v0
	v_mov_b32_e32 v72, v0
	v_mov_b32_e32 v73, v0
	v_mov_b32_e32 v74, v0
	v_mov_b32_e32 v75, v0
	v_mov_b32_e32 v76, v0
	v_mov_b32_e32 v77, v0
	v_mov_b32_e32 v78, v0
	v_mov_b32_e32 v79, v0
	v_mov_b32_e32 v88, v0
	v_mov_b32_e32 v89, v0
	v_mov_b32_e32 v90, v0
	v_mov_b32_e32 v91, v0
	v_mov_b32_e32 v92, v0
	v_mov_b32_e32 v93, v0
	v_mov_b32_e32 v94, v0
	v_mov_b32_e32 v95, v0
	v_mov_b32_e32 v104, v0
	v_mov_b32_e32 v105, v0
	v_mov_b32_e32 v106, v0
	v_mov_b32_e32 v107, v0
	v_mov_b32_e32 v108, v0
	v_mov_b32_e32 v109, v0
	v_mov_b32_e32 v110, v0
	v_mov_b32_e32 v111, v0
	v_mov_b32_e32 v120, v0
	v_mov_b32_e32 v121, v0
	v_mov_b32_e32 v122, v0
	v_mov_b32_e32 v123, v0
	v_mov_b32_e32 v124, v0
	v_mov_b32_e32 v125, v0
	v_mov_b32_e32 v126, v0
	v_mov_b32_e32 v127, v0
	.p2alignl 6, 3212836864

;     DI int nt(const Unit& u) const { return (u.aux & 8) ? PLED / 64 : ((u.aux & 4) ? (D_ / 2) / 64 : D_ / 64); }
; template <class Epi, class Sched, bool ALIGN_EPI, bool FP8 = false>
; DI void gemm_phase(LAS unsigned char* lds, const Gemm g, const Sched& S, const Epi& E) {
;     ...
; #pragma unroll
;         for (int a = 0; a < 2; ++a)
; #pragma unroll
;             for (int b = 0; b < 2; ++b)
; #pragma unroll
;                 for (int m = 0; m < 4; ++m)
; #pragma unroll
;                     for (int n = 0; n < 2; ++n) acc[a][b][m][n] = (f32x4){0.f, 0.f, 0.f, 0.f};
;         cur = nxt; cA = nA; cB = nB; ++ui;
;         if constexpr (sched_vark<Sched>::value) nt = S.nt(cur);
.LBB0_1684:
	s_add_u32 s90, s46, 0x100
	v_mov_b32_e32 v0, 0
	s_addc_u32 s91, s47, 0
	s_mov_b32 s92, -2
	v_mov_b32_e32 v1, v0
	v_mov_b32_e32 v2, v0
	v_mov_b32_e32 v3, v0
	v_mov_b32_e32 v4, v0
	v_mov_b32_e32 v5, v0
	v_mov_b32_e32 v6, v0
	v_mov_b32_e32 v7, v0
	v_mov_b32_e32 v8, v0
	v_mov_b32_e32 v9, v0
	v_mov_b32_e32 v10, v0
	v_mov_b32_e32 v11, v0
	v_mov_b32_e32 v12, v0
	v_mov_b32_e32 v13, v0
	v_mov_b32_e32 v14, v0
	v_mov_b32_e32 v15, v0
	v_mov_b32_e32 v24, v0
	v_mov_b32_e32 v25, v0
	v_mov_b32_e32 v26, v0
	v_mov_b32_e32 v27, v0
	v_mov_b32_e32 v28, v0
	v_mov_b32_e32 v29, v0
	v_mov_b32_e32 v30, v0
	v_mov_b32_e32 v31, v0
	v_mov_b32_e32 v40, v0
	v_mov_b32_e32 v41, v0
	v_mov_b32_e32 v42, v0
	v_mov_b32_e32 v43, v0
	v_mov_b32_e32 v44, v0
	v_mov_b32_e32 v45, v0
	v_mov_b32_e32 v46, v0
	v_mov_b32_e32 v47, v0
	v_mov_b32_e32 v16, v0
	v_mov_b32_e32 v17, v0
	v_mov_b32_e32 v18, v0
	v_mov_b32_e32 v19, v0
	v_mov_b32_e32 v20, v0
	v_mov_b32_e32 v21, v0
	v_mov_b32_e32 v22, v0
	v_mov_b32_e32 v23, v0
	v_mov_b32_e32 v32, v0
	v_mov_b32_e32 v33, v0
	v_mov_b32_e32 v34, v0
	v_mov_b32_e32 v35, v0
	v_mov_b32_e32 v36, v0
	v_mov_b32_e32 v37, v0
	v_mov_b32_e32 v38, v0
	v_mov_b32_e32 v39, v0
	v_mov_b32_e32 v48, v0
	v_mov_b32_e32 v49, v0
	v_mov_b32_e32 v50, v0
	v_mov_b32_e32 v51, v0
	v_mov_b32_e32 v52, v0
	v_mov_b32_e32 v53, v0
	v_mov_b32_e32 v54, v0
	v_mov_b32_e32 v55, v0
	v_mov_b32_e32 v56, v0
	v_mov_b32_e32 v57, v0
	v_mov_b32_e32 v58, v0
	v_mov_b32_e32 v59, v0
	v_mov_b32_e32 v60, v0
	v_mov_b32_e32 v61, v0
	v_mov_b32_e32 v62, v0
	v_mov_b32_e32 v63, v0
	v_mov_b32_e32 v64, v0
	v_mov_b32_e32 v65, v0
	v_mov_b32_e32 v66, v0
	v_mov_b32_e32 v67, v0
	v_mov_b32_e32 v68, v0
	v_mov_b32_e32 v69, v0
	v_mov_b32_e32 v70, v0
	v_mov_b32_e32 v71, v0
	v_mov_b32_e32 v72, v0
	v_mov_b32_e32 v73, v0
	v_mov_b32_e32 v74, v0
	v_mov_b32_e32 v75, v0
	v_mov_b32_e32 v76, v0
	v_mov_b32_e32 v77, v0
	v_mov_b32_e32 v78, v0
	v_mov_b32_e32 v79, v0
	v_mov_b32_e32 v88, v0
	v_mov_b32_e32 v89, v0
	v_mov_b32_e32 v90, v0
	v_mov_b32_e32 v91, v0
	v_mov_b32_e32 v92, v0
	v_mov_b32_e32 v93, v0
	v_mov_b32_e32 v94, v0
	v_mov_b32_e32 v95, v0
	v_mov_b32_e32 v104, v0
	v_mov_b32_e32 v105, v0
	v_mov_b32_e32 v106, v0
	v_mov_b32_e32 v107, v0
	v_mov_b32_e32 v108, v0
	v_mov_b32_e32 v109, v0
	v_mov_b32_e32 v110, v0
	v_mov_b32_e32 v111, v0
	v_mov_b32_e32 v80, v0
	v_mov_b32_e32 v81, v0
	v_mov_b32_e32 v82, v0
	v_mov_b32_e32 v83, v0
	v_mov_b32_e32 v84, v0
	v_mov_b32_e32 v85, v0
	v_mov_b32_e32 v86, v0
	v_mov_b32_e32 v87, v0
	v_mov_b32_e32 v96, v0
	v_mov_b32_e32 v97, v0
	v_mov_b32_e32 v98, v0
	v_mov_b32_e32 v99, v0
	v_mov_b32_e32 v100, v0
	v_mov_b32_e32 v101, v0
	v_mov_b32_e32 v102, v0
	v_mov_b32_e32 v103, v0
	v_mov_b32_e32 v112, v0
	v_mov_b32_e32 v113, v0
	v_mov_b32_e32 v114, v0
	v_mov_b32_e32 v115, v0
	v_mov_b32_e32 v116, v0
	v_mov_b32_e32 v117, v0
	v_mov_b32_e32 v118, v0
	v_mov_b32_e32 v119, v0
	v_mov_b32_e32 v120, v0
	v_mov_b32_e32 v121, v0
	v_mov_b32_e32 v122, v0
	v_mov_b32_e32 v123, v0
	v_mov_b32_e32 v124, v0
	v_mov_b32_e32 v125, v0
	v_mov_b32_e32 v126, v0
	v_mov_b32_e32 v127, v0
	.p2alignl 6, 3212836864

;     DI bool next(int i, Unit& u) const { u.aux = 0; return tile_map(i, nM, nN, G, c, u.pm, u.pn); }
;     DI size_t a_off(const Unit& u) const { return (size_t)u.pm * astep; }
;     DI size_t b_off(const Unit& u) const { return (size_t)u.pn * bstep; }
;     DI bool next(int i, Unit& u) const { int pn; u.aux = 0; if (!tile_map(i, NTOK / 256, 16, G, c, u.pm, pn)) return false; u.pn = pn < 8 ? pn : pn + 8; return true; }
;     DI size_t a_off(const Unit& u) const { return (size_t)u.pm * (256 * D_ * 2); }
;     DI size_t b_off(const Unit& u) const { return (size_t)u.pn * (256 * D_ * 2); }
;     DI bool next(int i, Unit& u) const { int pn2; if (!tile_map(i, NTOK / 256, 8, G, c, u.pm, pn2)) return false; u.pn = pn2 >> 1; u.aux = pn2 & 1; return true; }
;     DI size_t a_off(const Unit& u) const { return (size_t)u.pm * (256 * D_ * 2) + (size_t)u.aux * (D_ / 2 * 2); }
;     DI size_t b_off(const Unit& u) const { return (size_t)(12 + u.pn) * (256 * D_ * 2) + (size_t)u.aux * (D_ / 2 * 2); }
;     DI bool next(int i, Unit& u) const { u.aux = 0; return tile_map(i, 8, NTOK / 256, G, c, u.pm, u.pn); }
;     DI size_t a_off(const Unit& u) const { const int phys = u.pm < 4 ? 8 + u.pm : 20 + u.pm; return (size_t)phys * (256 * D_ * 2); }
;     DI size_t b_off(const Unit& u) const { return (size_t)u.pn * (256 * D_ * 2); }
;     DI int nt(const Unit& u) const { return (u.aux & 8) ? PLED / 64 : ((u.aux & 4) ? (D_ / 2) / 64 : D_ / 64); }
;     DI bool next(int i, Unit& u) const { u.aux = i & 1; return tile_map(i >> 1, NTOK / 256, D_ / 256, G, c, u.pm, u.pn); }
; template <class Epi, class Sched, bool ALIGN_EPI, bool FP8 = false>
; DI void gemm_phase(LAS unsigned char* lds, const Gemm g, const Sched& S, const Epi& E) {
;     ...
;         const bool has_next = S.next(ui + 1, nxt);
;         const char* nA = has_next ? (const char*)g.A + S.a_off(nxt) : cA; const char* nB = has_next ? (const char*)g.Bt + S.b_off(nxt) : cB;
;     ...
; #pragma unroll
;         for (int a = 0; a < 2; ++a)
; #pragma unroll
;             for (int b = 0; b < 2; ++b)
; #pragma unroll
;                 for (int m = 0; m < 4; ++m)
; #pragma unroll
;                     for (int n = 0; n < 2; ++n) acc[a][b][m][n] = (f32x4){0.f, 0.f, 0.f, 0.f};
;         cur = nxt; cA = nA; cB = nB; ++ui;
;         if constexpr (sched_vark<Sched>::value) nt = S.nt(cur);
.LBB0_1709:
	s_ashr_i32 s55, s54, 31
	s_lshl_b64 s[56:57], s[54:55], 20
	s_add_u32 s56, s36, s56
	s_addc_u32 s57, s37, s57
	s_and_b64 s[58:59], s[2:3], exec
	s_cselect_b32 s55, s57, s63
	s_cselect_b32 s94, s56, s62
	s_ashr_i32 s53, s52, 31
	s_lshl_b64 s[58:59], s[52:53], 20
	s_add_u32 s58, s39, s58
	s_addc_u32 s59, s72, s59
	s_and_b64 s[66:67], s[2:3], exec
	s_cselect_b32 s53, s59, s65
	s_cselect_b32 s95, s58, s64
	s_add_u32 s96, s64, 0x100
	v_mov_b32_e32 v0, 0
	s_addc_u32 s97, s65, 0
	s_mov_b32 vcc_lo, -2
	v_mov_b32_e32 v1, v0
	v_mov_b32_e32 v2, v0
	v_mov_b32_e32 v3, v0
	v_mov_b32_e32 v4, v0
	v_mov_b32_e32 v5, v0
	v_mov_b32_e32 v6, v0
	v_mov_b32_e32 v7, v0
	v_mov_b32_e32 v16, v0
	v_mov_b32_e32 v17, v0
	v_mov_b32_e32 v18, v0
	v_mov_b32_e32 v19, v0
	v_mov_b32_e32 v20, v0
	v_mov_b32_e32 v21, v0
	v_mov_b32_e32 v22, v0
	v_mov_b32_e32 v23, v0
	v_mov_b32_e32 v32, v0
	v_mov_b32_e32 v33, v0
	v_mov_b32_e32 v34, v0
	v_mov_b32_e32 v35, v0
	v_mov_b32_e32 v36, v0
	v_mov_b32_e32 v37, v0
	v_mov_b32_e32 v38, v0
	v_mov_b32_e32 v39, v0
	v_mov_b32_e32 v48, v0
	v_mov_b32_e32 v49, v0
	v_mov_b32_e32 v50, v0
	v_mov_b32_e32 v51, v0
	v_mov_b32_e32 v52, v0
	v_mov_b32_e32 v53, v0
	v_mov_b32_e32 v54, v0
	v_mov_b32_e32 v55, v0
	v_mov_b32_e32 v8, v0
	v_mov_b32_e32 v9, v0
	v_mov_b32_e32 v10, v0
	v_mov_b32_e32 v11, v0
	v_mov_b32_e32 v12, v0
	v_mov_b32_e32 v13, v0
	v_mov_b32_e32 v14, v0
	v_mov_b32_e32 v15, v0
	v_mov_b32_e32 v24, v0
	v_mov_b32_e32 v25, v0
	v_mov_b32_e32 v26, v0
	v_mov_b32_e32 v27, v0
	v_mov_b32_e32 v28, v0
	v_mov_b32_e32 v29, v0
	v_mov_b32_e32 v30, v0
	v_mov_b32_e32 v31, v0
	v_mov_b32_e32 v40, v0
	v_mov_b32_e32 v41, v0
	v_mov_b32_e32 v42, v0
	v_mov_b32_e32 v43, v0
	v_mov_b32_e32 v44, v0
	v_mov_b32_e32 v45, v0
	v_mov_b32_e32 v46, v0
	v_mov_b32_e32 v47, v0
	v_mov_b32_e32 v56, v0
	v_mov_b32_e32 v57, v0
	v_mov_b32_e32 v58, v0
	v_mov_b32_e32 v59, v0
	v_mov_b32_e32 v60, v0
	v_mov_b32_e32 v61, v0
	v_mov_b32_e32 v62, v0
	v_mov_b32_e32 v63, v0
	v_mov_b32_e32 v64, v0
	v_mov_b32_e32 v65, v0
	v_mov_b32_e32 v66, v0
	v_mov_b32_e32 v67, v0
	v_mov_b32_e32 v68, v0
	v_mov_b32_e32 v69, v0
	v_mov_b32_e32 v70, v0
	v_mov_b32_e32 v71, v0
	v_mov_b32_e32 v80, v0
	v_mov_b32_e32 v81, v0
	v_mov_b32_e32 v82, v0
	v_mov_b32_e32 v83, v0
	v_mov_b32_e32 v84, v0
	v_mov_b32_e32 v85, v0
	v_mov_b32_e32 v86, v0
	v_mov_b32_e32 v87, v0
	v_mov_b32_e32 v96, v0
	v_mov_b32_e32 v97, v0
	v_mov_b32_e32 v98, v0
	v_mov_b32_e32 v99, v0
	v_mov_b32_e32 v100, v0
	v_mov_b32_e32 v101, v0
	v_mov_b32_e32 v102, v0
	v_mov_b32_e32 v103, v0
	v_mov_b32_e32 v112, v0
	v_mov_b32_e32 v113, v0
	v_mov_b32_e32 v114, v0
	v_mov_b32_e32 v115, v0
	v_mov_b32_e32 v116, v0
	v_mov_b32_e32 v117, v0
	v_mov_b32_e32 v118, v0
	v_mov_b32_e32 v119, v0
	v_mov_b32_e32 v72, v0
	v_mov_b32_e32 v73, v0
	v_mov_b32_e32 v74, v0
	v_mov_b32_e32 v75, v0
	v_mov_b32_e32 v76, v0
	v_mov_b32_e32 v77, v0
	v_mov_b32_e32 v78, v0
	v_mov_b32_e32 v79, v0
	v_mov_b32_e32 v88, v0
	v_mov_b32_e32 v89, v0
	v_mov_b32_e32 v90, v0
	v_mov_b32_e32 v91, v0
	v_mov_b32_e32 v92, v0
	v_mov_b32_e32 v93, v0
	v_mov_b32_e32 v94, v0
	v_mov_b32_e32 v95, v0
	v_mov_b32_e32 v104, v0
	v_mov_b32_e32 v105, v0
	v_mov_b32_e32 v106, v0
	v_mov_b32_e32 v107, v0
	v_mov_b32_e32 v108, v0
	v_mov_b32_e32 v109, v0
	v_mov_b32_e32 v110, v0
	v_mov_b32_e32 v111, v0
	v_mov_b32_e32 v120, v0
	v_mov_b32_e32 v121, v0
	v_mov_b32_e32 v122, v0
	v_mov_b32_e32 v123, v0
	v_mov_b32_e32 v124, v0
	v_mov_b32_e32 v125, v0
	v_mov_b32_e32 v126, v0
	v_mov_b32_e32 v127, v0
	.p2alignl 6, 3212836864
